# baseline (speedup 1.0000x reference)
.Lec_skip:
	v_mul_u32_u24_e32 v4, 0x4080, v119
	s_waitcnt vmcnt(6)
	v_add3_u32 v5, v108, v4, s2
	v_lshl_or_b32 v4, v118, 2, v4
	s_mov_b64 s[2:3], 0x14280
	s_waitcnt lgkmcnt(0)
	s_barrier
	v_add_u32_e32 v4, 0x18400, v4
	v_lshl_add_u64 v[2:3], v[2:3], 0, s[2:3]
	ds_read_b128 v[88:91], v5
	ds_read_b128 v[84:87], v5 offset:1024
	ds_read_b128 v[80:83], v5 offset:2048
	ds_read_b128 v[76:79], v5 offset:3072
	ds_read_b128 v[72:75], v5 offset:4096
	ds_read_b128 v[68:71], v5 offset:5120
	ds_read_b128 v[64:67], v5 offset:6144
	ds_read_b128 v[60:63], v5 offset:7168
	ds_read_b128 v[56:59], v5 offset:8192
	ds_read_b128 v[52:55], v5 offset:9216
	ds_read_b128 v[48:51], v5 offset:10240
	ds_read_b128 v[44:47], v5 offset:11264
	ds_read_b128 v[40:43], v5 offset:12288
	ds_read_b128 v[36:39], v5 offset:13312
	ds_read_b128 v[32:35], v5 offset:14336
	ds_read_b128 v[28:31], v5 offset:15360
	ds_read_b32 v116, v4
	s_waitcnt lgkmcnt(0)
	v_lshl_add_u64 v[4:5], v[2:3], 0, v[6:7]
	v_add_u32_e32 v7, 0x14280, v6
	s_barrier
	v_readfirstlane_b32 s2, v7
	v_add_u32_e32 v7, 0x17280, v6
	s_mov_b32 m0, s2
	v_mov_b32_e32 v15, v109
	v_readfirstlane_b32 s2, v7
	v_add_u32_e32 v7, 0x1a280, v6
	global_load_lds_dwordx4 v[4:5], off
	v_lshl_add_u64 v[4:5], v[2:3], 0, v[14:15]
	s_mov_b32 m0, s2
	v_mov_b32_e32 v17, v109
	v_readfirstlane_b32 s2, v7
	v_add_u32_e32 v7, 0x1d280, v6
	global_load_lds_dwordx4 v[4:5], off
	v_lshl_add_u64 v[4:5], v[2:3], 0, v[16:17]
	s_mov_b32 m0, s2
	v_mov_b32_e32 v19, v109
	v_readfirstlane_b32 s2, v7
	global_load_lds_dwordx4 v[4:5], off
	v_lshl_add_u64 v[4:5], v[2:3], 0, v[18:19]
	s_mov_b32 m0, s2
	v_bfe_u32 v117, v0, 5, 1
	global_load_lds_dwordx4 v[4:5], off
	v_or_b32_e32 v4, 0xc000, v6
	v_add_u32_e32 v6, 0x20280, v6
	v_mov_b32_e32 v5, v109
	v_readfirstlane_b32 s2, v6
	v_lshl_add_u64 v[4:5], v[2:3], 0, v[4:5]
	s_mov_b32 m0, s2
	v_add_u32_e32 v131, 33, v115
	global_load_lds_dwordx4 v[4:5], off
	v_min_u32_e32 v4, 4, v27
	v_lshlrev_b32_e32 v6, 10, v4
	v_add_u32_e32 v4, 0xf000, v6
	v_mov_b32_e32 v5, v109
	v_lshl_add_u64 v[2:3], v[2:3], 0, v[4:5]
	v_add_u32_e32 v4, 0x23280, v6
	s_movk_i32 s73, 0x4080
	v_readfirstlane_b32 s2, v4
	s_mov_b32 m0, s2
	v_mov_b32_e32 v18, 0x7f800000
	global_load_lds_dwordx4 v[2:3], off
	v_lshrrev_b32_e32 v2, 1, v0
	v_and_b32_e32 v3, 3, v0
	v_and_or_b32 v2, v2, 12, v3
	v_cmp_eq_u32_e64 s[2:3], 0, v2
	v_cmp_eq_u32_e64 s[4:5], 1, v2
	v_cmp_eq_u32_e64 s[6:7], 2, v2
	v_cmp_eq_u32_e64 s[8:9], 3, v2
	v_cmp_eq_u32_e64 s[10:11], 4, v2
	v_cmp_eq_u32_e64 s[12:13], 5, v2
	v_cmp_eq_u32_e64 s[14:15], 6, v2
	v_cmp_eq_u32_e64 s[16:17], 7, v2
	v_cmp_eq_u32_e64 s[18:19], 8, v2
	v_cmp_eq_u32_e64 s[20:21], 9, v2
	v_cmp_eq_u32_e64 s[22:23], 10, v2
	v_cmp_eq_u32_e64 s[24:25], 11, v2
	v_cmp_eq_u32_e64 s[26:27], 12, v2
	v_cmp_eq_u32_e64 s[28:29], 13, v2
	v_cmp_eq_u32_e64 s[30:31], 14, v2
	v_cmp_eq_u32_e64 s[34:35], 15, v2
	v_mul_u32_u24_e32 v2, 0x4080, v115
	v_lshl_or_b32 v2, v117, 4, v2
	v_bfe_u32 v3, v0, 2, 1
	v_add_u32_e32 v132, 0x4000, v2
	v_lshl_or_b32 v2, s59, 2, v119
	v_cmp_eq_u32_e32 vcc, v117, v3
	v_sub_u32_e32 v3, s78, v115
	v_sub_u32_e32 v134, v2, v115
	v_add_u32_e32 v2, s72, v131
	v_cmp_lt_i32_e64 s[36:37], 0, v3
	v_cmp_lt_i32_e64 s[38:39], 3, v3
	v_cmp_lt_i32_e64 s[40:41], 6, v3
	v_cmp_lt_i32_e64 s[42:43], 9, v3
	v_cmp_lt_i32_e64 s[44:45], 12, v3
	v_cmp_lt_i32_e64 s[46:47], 15, v3
	v_cmp_lt_i32_e64 s[48:49], 18, v3
	v_cmp_lt_i32_e64 s[50:51], 21, v3
	v_cmp_lt_i32_e64 s[52:53], 24, v3
	v_cmp_lt_i32_e64 s[54:55], 27, v3
	v_cmp_lt_i32_e64 s[56:57], 30, v3
	v_ashrrev_i32_e32 v3, 31, v2
	v_lshlrev_b64 v[2:3], 10, v[2:3]
	v_lshl_or_b32 v2, v1, 2, v2
	v_lshl_add_u64 v[110:111], s[0:1], 0, v[108:109]
	v_cmp_gt_i32_e64 s[0:1], s78, v131
	s_and_b64 s[2:3], vcc, s[2:3]
	s_and_b64 s[4:5], vcc, s[4:5]
	s_and_b64 s[6:7], vcc, s[6:7]
	s_and_b64 s[8:9], vcc, s[8:9]
	s_and_b64 s[10:11], vcc, s[10:11]
	s_and_b64 s[12:13], vcc, s[12:13]
	s_and_b64 s[14:15], vcc, s[14:15]
	s_and_b64 s[16:17], vcc, s[16:17]
	s_and_b64 s[18:19], vcc, s[18:19]
	s_and_b64 s[20:21], vcc, s[20:21]
	s_and_b64 s[22:23], vcc, s[22:23]
	s_and_b64 s[24:25], vcc, s[24:25]
	s_and_b64 s[26:27], vcc, s[26:27]
	s_and_b64 s[28:29], vcc, s[28:29]
	s_and_b64 s[30:31], vcc, s[30:31]
	s_and_b64 s[34:35], vcc, s[34:35]
	v_mad_u32_u24 v133, v115, s73, v108
	v_lshl_add_u64 v[112:113], s[60:61], 0, v[2:3]
	s_mov_b64 s[60:61], -1
	v_mov_b32_e32 v135, 0x4080
	v_mov_b32_e32 v136, 0xff800000
	v_mov_b32_e32 v137, 0
	s_mov_b32 s81, s79
	v_mov_b32_e32 v1, v18
	v_mov_b32_e32 v20, v18
	v_mov_b32_e32 v19, v18
	v_mov_b32_e32 v24, v18
	v_mov_b32_e32 v23, v18
	v_mov_b32_e32 v22, v18
	v_mov_b32_e32 v21, v18
	v_mov_b32_e32 v26, v18
	v_mov_b32_e32 v25, v18
	s_waitcnt vmcnt(7)
	s_barrier
	s_and_b64 vcc, exec, s[68:69]
	s_cbranch_vccz .Led_skip
	v_readfirstlane_b32 s84, v115
	s_cmp_lg_u32 s84, 2
	s_cbranch_scc1 .Led_skip
	v_and_b32_e32 v14, 32, v0
	v_or_b32_e32 v15, 0x25400, v14
	v_mov_b32_e32 v2, 0
	v_mov_b32_e32 v3, 0
	v_mov_b32_e32 v4, 0
	v_mov_b32_e32 v5, 0
	ds_read_b128 v[92:95], v15 offset:0
	ds_read_b128 v[96:99], v15 offset:16
	ds_read_b128 v[100:103], v15 offset:64
	ds_read_b128 v[104:107], v15 offset:80
	ds_read_b128 v[142:145], v15 offset:128
	ds_read_b128 v[146:149], v15 offset:144
	ds_read_b128 v[150:153], v15 offset:192
	ds_read_b128 v[154:157], v15 offset:208
	s_waitcnt lgkmcnt(0)
	v_fma_mix_f32 v2, v88, v92, v2 op_sel:[0,0,0] op_sel_hi:[1,0,0]
	v_fma_mix_f32 v3, v84, v100, v3 op_sel:[0,0,0] op_sel_hi:[1,0,0]
	v_fma_mix_f32 v4, v80, v142, v4 op_sel:[0,0,0] op_sel_hi:[1,0,0]
	v_fma_mix_f32 v5, v76, v150, v5 op_sel:[0,0,0] op_sel_hi:[1,0,0]
	v_fma_mix_f32 v2, v88, v93, v2 op_sel:[1,0,0] op_sel_hi:[1,0,0]
	v_fma_mix_f32 v3, v84, v101, v3 op_sel:[1,0,0] op_sel_hi:[1,0,0]
	v_fma_mix_f32 v4, v80, v143, v4 op_sel:[1,0,0] op_sel_hi:[1,0,0]
	v_fma_mix_f32 v5, v76, v151, v5 op_sel:[1,0,0] op_sel_hi:[1,0,0]
	v_fma_mix_f32 v2, v89, v94, v2 op_sel:[0,0,0] op_sel_hi:[1,0,0]
	v_fma_mix_f32 v3, v85, v102, v3 op_sel:[0,0,0] op_sel_hi:[1,0,0]
	v_fma_mix_f32 v4, v81, v144, v4 op_sel:[0,0,0] op_sel_hi:[1,0,0]
	v_fma_mix_f32 v5, v77, v152, v5 op_sel:[0,0,0] op_sel_hi:[1,0,0]
	v_fma_mix_f32 v2, v89, v95, v2 op_sel:[1,0,0] op_sel_hi:[1,0,0]
	v_fma_mix_f32 v3, v85, v103, v3 op_sel:[1,0,0] op_sel_hi:[1,0,0]
	v_fma_mix_f32 v4, v81, v145, v4 op_sel:[1,0,0] op_sel_hi:[1,0,0]
	v_fma_mix_f32 v5, v77, v153, v5 op_sel:[1,0,0] op_sel_hi:[1,0,0]
	v_fma_mix_f32 v2, v90, v96, v2 op_sel:[0,0,0] op_sel_hi:[1,0,0]
	v_fma_mix_f32 v3, v86, v104, v3 op_sel:[0,0,0] op_sel_hi:[1,0,0]
	v_fma_mix_f32 v4, v82, v146, v4 op_sel:[0,0,0] op_sel_hi:[1,0,0]
	v_fma_mix_f32 v5, v78, v154, v5 op_sel:[0,0,0] op_sel_hi:[1,0,0]
	v_fma_mix_f32 v2, v90, v97, v2 op_sel:[1,0,0] op_sel_hi:[1,0,0]
	v_fma_mix_f32 v3, v86, v105, v3 op_sel:[1,0,0] op_sel_hi:[1,0,0]
	v_fma_mix_f32 v4, v82, v147, v4 op_sel:[1,0,0] op_sel_hi:[1,0,0]
	v_fma_mix_f32 v5, v78, v155, v5 op_sel:[1,0,0] op_sel_hi:[1,0,0]
	v_fma_mix_f32 v2, v91, v98, v2 op_sel:[0,0,0] op_sel_hi:[1,0,0]
	v_fma_mix_f32 v3, v87, v106, v3 op_sel:[0,0,0] op_sel_hi:[1,0,0]
	v_fma_mix_f32 v4, v83, v148, v4 op_sel:[0,0,0] op_sel_hi:[1,0,0]
	v_fma_mix_f32 v5, v79, v156, v5 op_sel:[0,0,0] op_sel_hi:[1,0,0]
	v_fma_mix_f32 v2, v91, v99, v2 op_sel:[1,0,0] op_sel_hi:[1,0,0]
	v_fma_mix_f32 v3, v87, v107, v3 op_sel:[1,0,0] op_sel_hi:[1,0,0]
	v_fma_mix_f32 v4, v83, v149, v4 op_sel:[1,0,0] op_sel_hi:[1,0,0]
	v_fma_mix_f32 v5, v79, v157, v5 op_sel:[1,0,0] op_sel_hi:[1,0,0]
	ds_read_b128 v[92:95], v15 offset:256
	ds_read_b128 v[96:99], v15 offset:272
	ds_read_b128 v[100:103], v15 offset:320
	ds_read_b128 v[104:107], v15 offset:336
	ds_read_b128 v[142:145], v15 offset:384
	ds_read_b128 v[146:149], v15 offset:400
	ds_read_b128 v[150:153], v15 offset:448
	ds_read_b128 v[154:157], v15 offset:464
	s_waitcnt lgkmcnt(0)
	v_fma_mix_f32 v2, v72, v92, v2 op_sel:[0,0,0] op_sel_hi:[1,0,0]
	v_fma_mix_f32 v3, v68, v100, v3 op_sel:[0,0,0] op_sel_hi:[1,0,0]
	v_fma_mix_f32 v4, v64, v142, v4 op_sel:[0,0,0] op_sel_hi:[1,0,0]
	v_fma_mix_f32 v5, v60, v150, v5 op_sel:[0,0,0] op_sel_hi:[1,0,0]
	v_fma_mix_f32 v2, v72, v93, v2 op_sel:[1,0,0] op_sel_hi:[1,0,0]
	v_fma_mix_f32 v3, v68, v101, v3 op_sel:[1,0,0] op_sel_hi:[1,0,0]
	v_fma_mix_f32 v4, v64, v143, v4 op_sel:[1,0,0] op_sel_hi:[1,0,0]
	v_fma_mix_f32 v5, v60, v151, v5 op_sel:[1,0,0] op_sel_hi:[1,0,0]
	v_fma_mix_f32 v2, v73, v94, v2 op_sel:[0,0,0] op_sel_hi:[1,0,0]
	v_fma_mix_f32 v3, v69, v102, v3 op_sel:[0,0,0] op_sel_hi:[1,0,0]
	v_fma_mix_f32 v4, v65, v144, v4 op_sel:[0,0,0] op_sel_hi:[1,0,0]
	v_fma_mix_f32 v5, v61, v152, v5 op_sel:[0,0,0] op_sel_hi:[1,0,0]
	v_fma_mix_f32 v2, v73, v95, v2 op_sel:[1,0,0] op_sel_hi:[1,0,0]
	v_fma_mix_f32 v3, v69, v103, v3 op_sel:[1,0,0] op_sel_hi:[1,0,0]
	v_fma_mix_f32 v4, v65, v145, v4 op_sel:[1,0,0] op_sel_hi:[1,0,0]
	v_fma_mix_f32 v5, v61, v153, v5 op_sel:[1,0,0] op_sel_hi:[1,0,0]
	v_fma_mix_f32 v2, v74, v96, v2 op_sel:[0,0,0] op_sel_hi:[1,0,0]
	v_fma_mix_f32 v3, v70, v104, v3 op_sel:[0,0,0] op_sel_hi:[1,0,0]
	v_fma_mix_f32 v4, v66, v146, v4 op_sel:[0,0,0] op_sel_hi:[1,0,0]
	v_fma_mix_f32 v5, v62, v154, v5 op_sel:[0,0,0] op_sel_hi:[1,0,0]
	v_fma_mix_f32 v2, v74, v97, v2 op_sel:[1,0,0] op_sel_hi:[1,0,0]
	v_fma_mix_f32 v3, v70, v105, v3 op_sel:[1,0,0] op_sel_hi:[1,0,0]
	v_fma_mix_f32 v4, v66, v147, v4 op_sel:[1,0,0] op_sel_hi:[1,0,0]
	v_fma_mix_f32 v5, v62, v155, v5 op_sel:[1,0,0] op_sel_hi:[1,0,0]
	v_fma_mix_f32 v2, v75, v98, v2 op_sel:[0,0,0] op_sel_hi:[1,0,0]
	v_fma_mix_f32 v3, v71, v106, v3 op_sel:[0,0,0] op_sel_hi:[1,0,0]
	v_fma_mix_f32 v4, v67, v148, v4 op_sel:[0,0,0] op_sel_hi:[1,0,0]
	v_fma_mix_f32 v5, v63, v156, v5 op_sel:[0,0,0] op_sel_hi:[1,0,0]
	v_fma_mix_f32 v2, v75, v99, v2 op_sel:[1,0,0] op_sel_hi:[1,0,0]
	v_fma_mix_f32 v3, v71, v107, v3 op_sel:[1,0,0] op_sel_hi:[1,0,0]
	v_fma_mix_f32 v4, v67, v149, v4 op_sel:[1,0,0] op_sel_hi:[1,0,0]
	v_fma_mix_f32 v5, v63, v157, v5 op_sel:[1,0,0] op_sel_hi:[1,0,0]
	ds_read_b128 v[92:95], v15 offset:512
	ds_read_b128 v[96:99], v15 offset:528
	ds_read_b128 v[100:103], v15 offset:576
	ds_read_b128 v[104:107], v15 offset:592
	ds_read_b128 v[142:145], v15 offset:640
	ds_read_b128 v[146:149], v15 offset:656
	ds_read_b128 v[150:153], v15 offset:704
	ds_read_b128 v[154:157], v15 offset:720
	s_waitcnt lgkmcnt(0)
	v_fma_mix_f32 v2, v56, v92, v2 op_sel:[0,0,0] op_sel_hi:[1,0,0]
	v_fma_mix_f32 v3, v52, v100, v3 op_sel:[0,0,0] op_sel_hi:[1,0,0]
	v_fma_mix_f32 v4, v48, v142, v4 op_sel:[0,0,0] op_sel_hi:[1,0,0]
	v_fma_mix_f32 v5, v44, v150, v5 op_sel:[0,0,0] op_sel_hi:[1,0,0]
	v_fma_mix_f32 v2, v56, v93, v2 op_sel:[1,0,0] op_sel_hi:[1,0,0]
	v_fma_mix_f32 v3, v52, v101, v3 op_sel:[1,0,0] op_sel_hi:[1,0,0]
	v_fma_mix_f32 v4, v48, v143, v4 op_sel:[1,0,0] op_sel_hi:[1,0,0]
	v_fma_mix_f32 v5, v44, v151, v5 op_sel:[1,0,0] op_sel_hi:[1,0,0]
	v_fma_mix_f32 v2, v57, v94, v2 op_sel:[0,0,0] op_sel_hi:[1,0,0]
	v_fma_mix_f32 v3, v53, v102, v3 op_sel:[0,0,0] op_sel_hi:[1,0,0]
	v_fma_mix_f32 v4, v49, v144, v4 op_sel:[0,0,0] op_sel_hi:[1,0,0]
	v_fma_mix_f32 v5, v45, v152, v5 op_sel:[0,0,0] op_sel_hi:[1,0,0]
	v_fma_mix_f32 v2, v57, v95, v2 op_sel:[1,0,0] op_sel_hi:[1,0,0]
	v_fma_mix_f32 v3, v53, v103, v3 op_sel:[1,0,0] op_sel_hi:[1,0,0]
	v_fma_mix_f32 v4, v49, v145, v4 op_sel:[1,0,0] op_sel_hi:[1,0,0]
	v_fma_mix_f32 v5, v45, v153, v5 op_sel:[1,0,0] op_sel_hi:[1,0,0]
	v_fma_mix_f32 v2, v58, v96, v2 op_sel:[0,0,0] op_sel_hi:[1,0,0]
	v_fma_mix_f32 v3, v54, v104, v3 op_sel:[0,0,0] op_sel_hi:[1,0,0]
	v_fma_mix_f32 v4, v50, v146, v4 op_sel:[0,0,0] op_sel_hi:[1,0,0]
	v_fma_mix_f32 v5, v46, v154, v5 op_sel:[0,0,0] op_sel_hi:[1,0,0]
	v_fma_mix_f32 v2, v58, v97, v2 op_sel:[1,0,0] op_sel_hi:[1,0,0]
	v_fma_mix_f32 v3, v54, v105, v3 op_sel:[1,0,0] op_sel_hi:[1,0,0]
	v_fma_mix_f32 v4, v50, v147, v4 op_sel:[1,0,0] op_sel_hi:[1,0,0]
	v_fma_mix_f32 v5, v46, v155, v5 op_sel:[1,0,0] op_sel_hi:[1,0,0]
	v_fma_mix_f32 v2, v59, v98, v2 op_sel:[0,0,0] op_sel_hi:[1,0,0]
	v_fma_mix_f32 v3, v55, v106, v3 op_sel:[0,0,0] op_sel_hi:[1,0,0]
	v_fma_mix_f32 v4, v51, v148, v4 op_sel:[0,0,0] op_sel_hi:[1,0,0]
	v_fma_mix_f32 v5, v47, v156, v5 op_sel:[0,0,0] op_sel_hi:[1,0,0]
	v_fma_mix_f32 v2, v59, v99, v2 op_sel:[1,0,0] op_sel_hi:[1,0,0]
	v_fma_mix_f32 v3, v55, v107, v3 op_sel:[1,0,0] op_sel_hi:[1,0,0]
	v_fma_mix_f32 v4, v51, v149, v4 op_sel:[1,0,0] op_sel_hi:[1,0,0]
	v_fma_mix_f32 v5, v47, v157, v5 op_sel:[1,0,0] op_sel_hi:[1,0,0]
	ds_read_b128 v[92:95], v15 offset:768
	ds_read_b128 v[96:99], v15 offset:784
	ds_read_b128 v[100:103], v15 offset:832
	ds_read_b128 v[104:107], v15 offset:848
	ds_read_b128 v[142:145], v15 offset:896
	ds_read_b128 v[146:149], v15 offset:912
	ds_read_b128 v[150:153], v15 offset:960
	ds_read_b128 v[154:157], v15 offset:976
	s_waitcnt lgkmcnt(0)
	v_fma_mix_f32 v2, v40, v92, v2 op_sel:[0,0,0] op_sel_hi:[1,0,0]
	v_fma_mix_f32 v3, v36, v100, v3 op_sel:[0,0,0] op_sel_hi:[1,0,0]
	v_fma_mix_f32 v4, v32, v142, v4 op_sel:[0,0,0] op_sel_hi:[1,0,0]
	v_fma_mix_f32 v5, v28, v150, v5 op_sel:[0,0,0] op_sel_hi:[1,0,0]
	v_fma_mix_f32 v2, v40, v93, v2 op_sel:[1,0,0] op_sel_hi:[1,0,0]
	v_fma_mix_f32 v3, v36, v101, v3 op_sel:[1,0,0] op_sel_hi:[1,0,0]
	v_fma_mix_f32 v4, v32, v143, v4 op_sel:[1,0,0] op_sel_hi:[1,0,0]
	v_fma_mix_f32 v5, v28, v151, v5 op_sel:[1,0,0] op_sel_hi:[1,0,0]
	v_fma_mix_f32 v2, v41, v94, v2 op_sel:[0,0,0] op_sel_hi:[1,0,0]
	v_fma_mix_f32 v3, v37, v102, v3 op_sel:[0,0,0] op_sel_hi:[1,0,0]
	v_fma_mix_f32 v4, v33, v144, v4 op_sel:[0,0,0] op_sel_hi:[1,0,0]
	v_fma_mix_f32 v5, v29, v152, v5 op_sel:[0,0,0] op_sel_hi:[1,0,0]
	v_fma_mix_f32 v2, v41, v95, v2 op_sel:[1,0,0] op_sel_hi:[1,0,0]
	v_fma_mix_f32 v3, v37, v103, v3 op_sel:[1,0,0] op_sel_hi:[1,0,0]
	v_fma_mix_f32 v4, v33, v145, v4 op_sel:[1,0,0] op_sel_hi:[1,0,0]
	v_fma_mix_f32 v5, v29, v153, v5 op_sel:[1,0,0] op_sel_hi:[1,0,0]
	v_fma_mix_f32 v2, v42, v96, v2 op_sel:[0,0,0] op_sel_hi:[1,0,0]
	v_fma_mix_f32 v3, v38, v104, v3 op_sel:[0,0,0] op_sel_hi:[1,0,0]
	v_fma_mix_f32 v4, v34, v146, v4 op_sel:[0,0,0] op_sel_hi:[1,0,0]
	v_fma_mix_f32 v5, v30, v154, v5 op_sel:[0,0,0] op_sel_hi:[1,0,0]
	v_fma_mix_f32 v2, v42, v97, v2 op_sel:[1,0,0] op_sel_hi:[1,0,0]
	v_fma_mix_f32 v3, v38, v105, v3 op_sel:[1,0,0] op_sel_hi:[1,0,0]
	v_fma_mix_f32 v4, v34, v147, v4 op_sel:[1,0,0] op_sel_hi:[1,0,0]
	v_fma_mix_f32 v5, v30, v155, v5 op_sel:[1,0,0] op_sel_hi:[1,0,0]
	v_fma_mix_f32 v2, v43, v98, v2 op_sel:[0,0,0] op_sel_hi:[1,0,0]
	v_fma_mix_f32 v3, v39, v106, v3 op_sel:[0,0,0] op_sel_hi:[1,0,0]
	v_fma_mix_f32 v4, v35, v148, v4 op_sel:[0,0,0] op_sel_hi:[1,0,0]
	v_fma_mix_f32 v5, v31, v156, v5 op_sel:[0,0,0] op_sel_hi:[1,0,0]
	v_fma_mix_f32 v2, v43, v99, v2 op_sel:[1,0,0] op_sel_hi:[1,0,0]
	v_fma_mix_f32 v3, v39, v107, v3 op_sel:[1,0,0] op_sel_hi:[1,0,0]
	v_fma_mix_f32 v4, v35, v149, v4 op_sel:[1,0,0] op_sel_hi:[1,0,0]
	v_fma_mix_f32 v5, v31, v157, v5 op_sel:[1,0,0] op_sel_hi:[1,0,0]
	v_add_f32_e32 v2, v2, v3
	v_add_f32_e32 v4, v4, v5
	v_add_f32_e32 v6, v2, v4
	v_mov_b32_e32 v2, 0x25830
	ds_read_b128 v[8:11], v2
	v_lshl_or_b32 v16, v119, 5, v118
	v_or_b32_e32 v16, s33, v16
	s_mov_b32 s84, 0xf800000
	v_cmp_gt_u32_e64 s[90:91], 32, v114
	v_mov_b32_e32 v7, v6
	v_mov_b32_e32 v12, v6
	s_nop 1
	v_permlane32_swap_b32_e32 v7, v12
	v_cmp_eq_u32_e32 vcc, v7, v6
	v_mov_b32_e32 v17, v116
	s_waitcnt lgkmcnt(0)
	v_add_f32_e32 v2, v9, v8
	v_add_f32_e32 v3, v10, v11
	v_cndmask_b32_e32 v7, v7, v12, vcc
	v_add_f32_e32 v6, v6, v7
	v_add_f32_e32 v2, v2, v3
	v_fmac_f32_e32 v17, -2.0, v6
	v_add_f32_e32 v2, v2, v17
	v_max_f32_e32 v2, 0, v2
	v_mul_f32_e32 v3, 0x4f800000, v2
	v_cmp_gt_f32_e32 vcc, s84, v2
	v_cmp_gt_i32_e64 s[86:87], s58, v16
	s_nop 0
	v_cndmask_b32_e32 v2, v2, v3, vcc
	v_sqrt_f32_e32 v3, v2
	s_nop 0
	v_add_u32_e32 v16, -1, v3
	v_fma_f32 v4, -v16, v3, v2
	v_cmp_ge_f32_e64 s[88:89], 0, v4
	v_add_u32_e32 v4, 1, v3
	s_nop 0
	v_cndmask_b32_e64 v16, v3, v16, s[88:89]
	v_fma_f32 v3, -v4, v3, v2
	v_cmp_lt_f32_e64 s[88:89], 0, v3
	s_nop 1
	v_cndmask_b32_e64 v16, v16, v4, s[88:89]
	v_mul_f32_e32 v3, 0x37800000, v16
	v_cndmask_b32_e32 v16, v16, v3, vcc
	v_mov_b32_e32 v3, 0x260
	v_cmp_class_f32_e32 vcc, v2, v3
	s_nop 1
	v_cndmask_b32_e32 v16, v16, v2, vcc
	s_and_b64 vcc, s[86:87], s[90:91]
	v_cndmask_b32_e32 v16, 0, v16, vcc
	s_nop 1
	v_add_f32_dpp v16, v16, v16 quad_perm:[1,0,3,2] row_mask:0xf bank_mask:0xf bound_ctrl:1
	s_nop 1
	v_add_f32_dpp v16, v16, v16 quad_perm:[2,3,0,1] row_mask:0xf bank_mask:0xf bound_ctrl:1
	s_nop 1
	v_add_f32_dpp v16, v16, v16 row_half_mirror row_mask:0xf bank_mask:0xf bound_ctrl:1
	s_nop 1
	v_add_f32_dpp v16, v16, v16 row_mirror row_mask:0xf bank_mask:0xf bound_ctrl:1
	s_nop 0
	v_readlane_b32 s94, v16, 16
	v_readlane_b32 s95, v16, 48
	v_readlane_b32 s92, v16, 0
	v_readlane_b32 s93, v16, 32
	v_mov_b32_e32 v2, s94
	v_mov_b32_e32 v3, s95
	v_pk_add_f32 v[2:3], s[92:93], v[2:3]
	s_nop 0
	v_add_f32_e32 v2, v2, v3
	v_cmp_eq_u32_e32 vcc, 0, v114
	s_and_saveexec_b64 s[84:85], vcc
	v_mov_b32_e32 v3, 0x25800
	v_lshl_add_u32 v3, v27, 2, v3
	ds_write_b32 v3, v2
	s_mov_b64 exec, s[84:85]

.LBB1_39:
	s_or_b64 exec, exec, s[2:3]
	s_andn2_b64 vcc, exec, s[68:69]
	s_cbranch_vccnz .LBB1_46
	v_cmp_eq_u32_e32 vcc, 0, v0
	s_and_saveexec_b64 s[0:1], vcc
	s_cbranch_execz .LBB1_46
	v_mov_b32_e32 v0, 0x25820
	ds_read_b128 v[0:3], v0
	s_lshl_b32 s0, s8, 6
	s_add_i32 s0, s0, s59
	s_ashr_i32 s1, s0, 31
	s_lshl_b64 s[0:1], s[0:1], 2
	s_waitcnt lgkmcnt(0)
	v_add_f32_e32 v0, v0, v1
	v_add_f32_e32 v0, v0, v2
	s_add_u32 s0, s66, s0
	v_add_f32_e32 v0, v0, v3
	s_addc_u32 s1, s67, s1
	v_mov_b32_e32 v1, 0
	global_store_dword v1, v0, s[0:1]
